# indexer step 1: remaining 4 of 16 scores per tile also keyed with packed 16-bit ops on the non-diagonal path (scalar key build moved into the rarely taken diagonal path)
# speedup vs baseline: 1.0117x; 1.0029x over previous
.LBB0_382:
	s_cmp_eq_u32 s81, s0
	s_mov_b64 s[0:1], -1
	v_mfma_f32_32x32x16_bf16 v[10:25], v[80:83], v[84:87], 0
	v_mfma_f32_32x32x16_bf16 v[10:25], v[76:79], v[88:91], v[10:25]
	v_mfma_f32_32x32x16_bf16 v[10:25], v[72:75], v[92:95], v[10:25]
	v_mfma_f32_32x32x16_bf16 v[10:25], v[52:55], v[96:99], v[10:25]
	s_nop 11
	v_fma_f32 v48, |v10|, v2, 0
	v_fma_f32 v49, |v11|, v2, 0
	v_fma_f32 v50, |v12|, v2, 0
	v_fma_f32 v51, |v13|, v2, 0
	v_fma_f32 v212, |v14|, v2, 0
	v_fma_f32 v213, |v15|, v2, 0
	v_fma_f32 v215, |v16|, v2, 0
	v_fma_f32 v216, |v17|, v2, 0
	v_fma_f32 v217, |v18|, v2, 0
	v_fma_f32 v228, |v19|, v2, 0
	v_mfma_f32_32x32x16_bf16 v[4:19], v[80:83], v[100:103], 0
	v_fma_f32 v229, |v20|, v2, 0
	v_fma_f32 v230, |v21|, v2, 0
	v_mfma_f32_32x32x16_bf16 v[4:19], v[76:79], v[104:107], v[4:19]
	v_fma_f32 v234, |v22|, v2, 0
	v_fma_f32 v235, |v23|, v2, 0
	v_mfma_f32_32x32x16_bf16 v[4:19], v[72:75], v[108:111], v[4:19]
	v_fma_f32 v236, |v24|, v2, 0
	v_fma_f32 v237, |v25|, v2, 0
	v_mfma_f32_32x32x16_bf16 v[4:19], v[52:55], v[112:115], v[4:19]
	s_nop 11
	v_fma_f32 v48, |v4|, v249, v48
	v_mfma_f32_32x32x16_bf16 v[20:35], v[80:83], v[116:119], 0
	v_fma_f32 v49, |v5|, v249, v49
	v_fma_f32 v50, |v6|, v249, v50
	v_fma_f32 v51, |v7|, v249, v51
	v_mfma_f32_32x32x16_bf16 v[20:35], v[76:79], v[120:123], v[20:35]
	v_fma_f32 v8, |v8|, v249, v212
	v_fma_f32 v9, |v9|, v249, v213
	v_fma_f32 v10, |v10|, v249, v215
	v_fma_f32 v11, |v11|, v249, v216
	v_mfma_f32_32x32x16_bf16 v[20:35], v[72:75], v[124:127], v[20:35]
	v_fma_f32 v12, |v12|, v249, v217
	v_fma_f32 v13, |v13|, v249, v228
	v_fma_f32 v212, |v14|, v249, v229
	v_fma_f32 v213, |v15|, v249, v230
	v_fma_f32 v215, |v16|, v249, v234
	v_fma_f32 v216, |v17|, v249, v235
	v_fma_f32 v217, |v18|, v249, v236
	v_fma_f32 v228, |v19|, v249, v237
	v_mfma_f32_32x32x16_bf16 v[20:35], v[52:55], v[128:131], v[20:35]
	s_nop 11
	v_fma_f32 v24, |v24|, v250, v8
	v_fma_f32 v25, |v25|, v250, v9
	v_fma_f32 v26, |v26|, v250, v10
	v_fma_f32 v27, |v27|, v250, v11
	v_fma_f32 v28, |v28|, v250, v12
	v_fma_f32 v29, |v29|, v250, v13
	v_mfma_f32_32x32x16_bf16 v[4:19], v[80:83], v[132:135], 0
	v_fma_f32 v48, |v20|, v250, v48
	v_fma_f32 v49, |v21|, v250, v49
	v_fma_f32 v50, |v22|, v250, v50
	v_fma_f32 v51, |v23|, v250, v51
	v_mfma_f32_32x32x16_bf16 v[4:19], v[76:79], v[136:139], v[4:19]
	v_fma_f32 v212, |v30|, v250, v212
	v_mfma_f32_32x32x16_bf16 v[4:19], v[72:75], v[140:143], v[4:19]
	v_fma_f32 v213, |v31|, v250, v213
	v_fma_f32 v215, |v32|, v250, v215
	v_fma_f32 v216, |v33|, v250, v216
	v_fma_f32 v217, |v34|, v250, v217
	v_fma_f32 v228, |v35|, v250, v228
	v_mfma_f32_32x32x16_bf16 v[4:19], v[52:55], v[144:147], v[4:19]
	s_nop 11
	v_fma_f32 v229, |v8|, v251, v24
	v_fma_f32 v230, |v9|, v251, v25
	v_fma_f32 v234, |v10|, v251, v26
	v_fma_f32 v235, |v11|, v251, v27
	v_fma_f32 v236, |v12|, v251, v28
	v_fma_f32 v237, |v13|, v251, v29
	v_mfma_f32_32x32x16_bf16 v[20:35], v[80:83], v[148:151], 0
	v_fma_f32 v48, |v4|, v251, v48
	v_fma_f32 v49, |v5|, v251, v49
	v_fma_f32 v50, |v6|, v251, v50
	v_fma_f32 v51, |v7|, v251, v51
	v_mfma_f32_32x32x16_bf16 v[20:35], v[76:79], v[152:155], v[20:35]
	v_fma_f32 v212, |v14|, v251, v212
	v_mfma_f32_32x32x16_bf16 v[20:35], v[72:75], v[156:159], v[20:35]
	v_fma_f32 v213, |v15|, v251, v213
	v_fma_f32 v215, |v16|, v251, v215
	v_fma_f32 v216, |v17|, v251, v216
	v_fma_f32 v217, |v18|, v251, v217
	v_fma_f32 v228, |v19|, v251, v228
	v_mfma_f32_32x32x16_bf16 v[20:35], v[52:55], v[160:163], v[20:35]
	s_nop 11
	v_fma_f32 v20, |v20|, v252, v48
	v_fma_f32 v21, |v21|, v252, v49
	v_fma_f32 v22, |v22|, v252, v50
	v_fma_f32 v23, |v23|, v252, v51
	v_mfma_f32_32x32x16_bf16 v[36:51], v[80:83], v[164:167], 0
	v_fma_f32 v24, |v24|, v252, v229
	v_fma_f32 v25, |v25|, v252, v230
	v_mfma_f32_32x32x16_bf16 v[36:51], v[76:79], v[168:171], v[36:51]
	v_fma_f32 v26, |v26|, v252, v234
	v_fma_f32 v27, |v27|, v252, v235
	v_mfma_f32_32x32x16_bf16 v[36:51], v[72:75], v[172:175], v[36:51]
	v_fma_f32 v229, |v28|, v252, v236
	v_fma_f32 v230, |v29|, v252, v237
	v_fma_f32 v212, |v30|, v252, v212
	v_fma_f32 v213, |v31|, v252, v213
	v_fma_f32 v215, |v32|, v252, v215
	v_fma_f32 v216, |v33|, v252, v216
	v_fma_f32 v217, |v34|, v252, v217
	v_fma_f32 v228, |v35|, v252, v228
	v_mfma_f32_32x32x16_bf16 v[36:51], v[52:55], v[176:179], v[36:51]
	s_nop 11
	v_fma_f32 v234, |v36|, v253, v20
	v_fma_f32 v235, |v37|, v253, v21
	v_fma_f32 v236, |v38|, v253, v22
	v_fma_f32 v237, |v39|, v253, v23
	v_fma_f32 v40, |v40|, v253, v24
	v_fma_f32 v41, |v41|, v253, v25
	v_fma_f32 v42, |v42|, v253, v26
	v_fma_f32 v43, |v43|, v253, v27
	v_mfma_f32_32x32x16_bf16 v[12:27], v[80:83], v[180:183], 0
	v_fma_f32 v44, |v44|, v253, v229
	v_fma_f32 v45, |v45|, v253, v230
	v_mfma_f32_32x32x16_bf16 v[12:27], v[76:79], v[184:187], v[12:27]
	v_fma_f32 v46, |v46|, v253, v212
	v_fma_f32 v47, |v47|, v253, v213
	v_mfma_f32_32x32x16_bf16 v[12:27], v[72:75], v[188:191], v[12:27]
	v_fma_f32 v48, |v48|, v253, v215
	v_fma_f32 v49, |v49|, v253, v216
	v_fma_f32 v50, |v50|, v253, v217
	v_fma_f32 v51, |v51|, v253, v228
	v_mfma_f32_32x32x16_bf16 v[12:27], v[52:55], v[192:195], v[12:27]
	s_nop 11
	v_fma_f32 v212, |v12|, v223, v234
	v_fma_f32 v213, |v13|, v223, v235
	v_fma_f32 v215, |v14|, v223, v236
	v_fma_f32 v216, |v15|, v223, v237
	v_fma_f32 v217, |v16|, v223, v40
	v_fma_f32 v228, |v17|, v223, v41
	v_fma_f32 v229, |v18|, v223, v42
	v_fma_f32 v230, |v19|, v223, v43
	v_mfma_f32_32x32x16_bf16 v[4:19], v[80:83], v[196:199], 0
	v_fma_f32 v234, |v20|, v223, v44
	v_fma_f32 v235, |v21|, v223, v45
	v_mfma_f32_32x32x16_bf16 v[4:19], v[76:79], v[200:203], v[4:19]
	v_fma_f32 v236, |v22|, v223, v46
	v_fma_f32 v237, |v23|, v223, v47
	v_mfma_f32_32x32x16_bf16 v[4:19], v[72:75], v[204:207], v[4:19]
	v_fma_f32 v48, |v24|, v223, v48
	v_fma_f32 v49, |v25|, v223, v49
	v_fma_f32 v50, |v26|, v223, v50
	v_fma_f32 v51, |v27|, v223, v51
	v_mfma_f32_32x32x16_bf16 v[4:19], v[52:55], v[208:211], v[4:19]
	ds_read_b128 v[20:23], v214 offset:32768
	ds_read_b128 v[36:39], v214 offset:33792
	ds_read_b128 v[40:43], v214 offset:34816
	ds_read_b128 v[44:47], v214 offset:35840
	s_waitcnt lgkmcnt(3)
	v_mfma_f32_32x32x16_bf16 v[20:35], v[80:83], v[20:23], 0
	s_nop 5
	v_fma_f32 v212, |v4|, v219, v212
	v_fma_f32 v213, |v5|, v219, v213
	v_fma_f32 v4, |v6|, v219, v215
	v_fma_f32 v5, |v7|, v219, v216
	s_waitcnt lgkmcnt(2)
	v_mfma_f32_32x32x16_bf16 v[20:35], v[76:79], v[36:39], v[20:35]
	v_fma_f32 v6, |v8|, v219, v217
	v_fma_f32 v7, |v9|, v219, v228
	v_fma_f32 v8, |v10|, v219, v229
	v_fma_f32 v9, |v11|, v219, v230
	s_waitcnt lgkmcnt(1)
	v_mfma_f32_32x32x16_bf16 v[20:35], v[72:75], v[40:43], v[20:35]
	v_fma_f32 v36, |v12|, v219, v234
	v_fma_f32 v37, |v13|, v219, v235
	v_fma_f32 v38, |v14|, v219, v236
	v_fma_f32 v39, |v15|, v219, v237
	s_waitcnt lgkmcnt(0)
	v_mfma_f32_32x32x16_bf16 v[20:35], v[52:55], v[44:47], v[20:35]
	v_fma_f32 v16, |v16|, v219, v48
	v_fma_f32 v17, |v17|, v219, v49
	s_nop 9
	v_add_f32_e32 v20, v212, v20
	v_pk_add_f32 v[14:15], v[4:5], v[22:23]
	v_pk_add_f32 v[4:5], v[32:33], v[16:17]
	v_cvt_f16_f32_e32 v16, v20
	v_fma_f32 v18, |v18|, v219, v50
	v_fma_f32 v19, |v19|, v219, v51
	v_add_f32_e32 v21, v213, v21
	v_add_f32_e32 v17, v34, v18
	v_add_f32_e32 v19, v35, v19
	v_pk_add_f32 v[10:11], v[8:9], v[26:27]
	v_pk_add_f32 v[8:9], v[36:37], v[28:29]
	v_cvt_f16_f32_e32 v29, v21
	v_cvt_f16_f32_e32 v18, v17
	v_cvt_f16_f32_e32 v17, v19
	v_pk_add_f32 v[12:13], v[6:7], v[24:25]
	v_pk_add_f32 v[6:7], v[38:39], v[30:31]
	s_cbranch_scc1 .LBB0_384
	s_mov_b64 s[0:1], 0
	v_cvt_pk_f16_f32 v23, v6, v7
	v_pk_ashrrev_i16 v24, 15, v23 op_sel_hi:[0,1]
	v_bitop3_b32 v7, v23, v24, s32 bitop3:0x1e
	v_bfe_u32 v24, v7, 8, 8
	v_lshrrev_b32_e32 v23, 24, v7
	v_lshl_add_u32 v24, v24, 2, v222
	v_lshl_add_u32 v23, v23, 2, v222
	ds_add_u32 v24, v224 offset:36864
	ds_add_u32 v23, v224 offset:36864
	v_cvt_pk_f16_f32 v25, v8, v9
	v_pk_ashrrev_i16 v27, 15, v25 op_sel_hi:[0,1]
	v_bitop3_b32 v6, v25, v27, s32 bitop3:0x1e
	v_bfe_u32 v27, v6, 8, 8
	v_lshrrev_b32_e32 v25, 24, v6
	v_lshl_add_u32 v27, v27, 2, v222
	v_lshl_add_u32 v25, v25, 2, v222
	ds_add_u32 v27, v224 offset:36864
	ds_add_u32 v25, v224 offset:36864
	v_cvt_pk_f16_f32 v28, v10, v11
	v_pk_ashrrev_i16 v32, 15, v28 op_sel_hi:[0,1]
	v_bitop3_b32 v9, v28, v32, s32 bitop3:0x1e
	v_bfe_u32 v32, v9, 8, 8
	v_lshrrev_b32_e32 v28, 24, v9
	v_lshl_add_u32 v32, v32, 2, v222
	v_lshl_add_u32 v28, v28, 2, v222
	ds_add_u32 v32, v224 offset:36864
	ds_add_u32 v28, v224 offset:36864
	v_cvt_pk_f16_f32 v33, v12, v13
	v_pk_ashrrev_i16 v34, 15, v33 op_sel_hi:[0,1]
	v_bitop3_b32 v8, v33, v34, s32 bitop3:0x1e
	v_bfe_u32 v34, v8, 8, 8
	v_lshrrev_b32_e32 v33, 24, v8
	v_lshl_add_u32 v34, v34, 2, v222
	v_lshl_add_u32 v33, v33, 2, v222
	ds_add_u32 v34, v224 offset:36864
	ds_add_u32 v33, v224 offset:36864
	v_cvt_pk_f16_f32 v35, v4, v5
	v_pk_ashrrev_i16 v36, 15, v35 op_sel_hi:[0,1]
	v_bitop3_b32 v10, v35, v36, s32 bitop3:0x1e
	v_bfe_u32 v36, v10, 8, 8
	v_lshrrev_b32_e32 v35, 24, v10
	v_lshl_add_u32 v36, v36, 2, v222
	v_lshl_add_u32 v35, v35, 2, v222
	ds_add_u32 v36, v224 offset:36864
	ds_add_u32 v35, v224 offset:36864
	v_cvt_pk_f16_f32 v37, v14, v15
	v_pk_ashrrev_i16 v39, 15, v37 op_sel_hi:[0,1]
	v_bitop3_b32 v5, v37, v39, s32 bitop3:0x1e
	v_bfe_u32 v39, v5, 8, 8
	v_lshrrev_b32_e32 v37, 24, v5
	v_lshl_add_u32 v39, v39, 2, v222
	v_lshl_add_u32 v37, v37, 2, v222
	ds_add_u32 v39, v224 offset:36864
	ds_add_u32 v37, v224 offset:36864
	v_lshl_or_b32 v23, v29, 16, v16
	v_lshl_or_b32 v25, v17, 16, v18
	v_pk_ashrrev_i16 v24, 15, v23 op_sel_hi:[0,1]
	v_pk_ashrrev_i16 v27, 15, v25 op_sel_hi:[0,1]
	v_bitop3_b32 v4, v23, v24, s32 bitop3:0x1e
	v_bitop3_b32 v11, v25, v27, s32 bitop3:0x1e
	v_bfe_u32 v23, v4, 8, 8
	v_lshrrev_b32_e32 v24, 24, v4
	v_bfe_u32 v25, v11, 8, 8
	v_lshrrev_b32_e32 v27, 24, v11
	v_lshl_add_u32 v23, v23, 2, v222
	v_lshl_add_u32 v24, v24, 2, v222
	v_lshl_add_u32 v25, v25, 2, v222
	v_lshl_add_u32 v27, v27, 2, v222
	ds_add_u32 v23, v224 offset:36864
	ds_add_u32 v24, v224 offset:36864
	ds_add_u32 v25, v224 offset:36864
	ds_add_u32 v27, v224 offset:36864
	s_branch .Lidx_join
.LBB0_384:
	s_andn2_b64 vcc, exec, s[0:1]
	s_cbranch_vccnz .LBB0_386
	v_bitop3_b32 v42, v16, s7, v16 bitop3:0xc
	v_or_b32_e32 v41, 0x8000, v16
	v_cmp_gt_i16_e32 vcc, 0, v16
	v_bitop3_b32 v30, v29, s7, v29 bitop3:0xc
	v_or_b32_e32 v31, 0x8000, v29
	v_cndmask_b32_e32 v26, v41, v42, vcc
	v_cmp_gt_i16_e64 s[60:61], 0, v29
	v_bitop3_b32 v21, v18, s7, v18 bitop3:0xc
	v_or_b32_e32 v22, 0x8000, v18
	v_cmp_gt_i16_e64 s[58:59], 0, v18
	v_bitop3_b32 v19, v17, s7, v17 bitop3:0xc
	v_or_b32_e32 v20, 0x8000, v17
	v_lshrrev_b32_e32 v16, 8, v26
	v_cndmask_b32_e64 v16, v16, v233, s[24:25]
	v_cmp_gt_i16_e32 vcc, 0, v29
	v_lshl_add_u32 v16, v16, 2, v222
	v_cvt_f16_f32_e32 v14, v14
	v_cndmask_b32_e32 v23, v31, v30, vcc
	ds_add_u32 v16, v224 offset:36864
	v_cndmask_b32_e64 v16, 0, v23, s[26:27]
	v_lshrrev_b32_e32 v23, 8, v23
	v_cndmask_b32_e64 v23, v233, v23, s[26:27]
	v_lshl_add_u32 v23, v23, 2, v222
	ds_add_u32 v23, v224 offset:36864
	v_bitop3_b32 v23, v14, s7, v14 bitop3:0xc
	v_or_b32_e32 v24, 0x8000, v14
	v_cmp_gt_i16_e32 vcc, 0, v14
	v_cvt_f16_f32_e32 v15, v15
	v_cvt_f16_f32_e32 v12, v12
	v_cndmask_b32_e32 v14, v24, v23, vcc
	v_cndmask_b32_e64 v23, v14, 0, s[28:29]
	v_lshrrev_b32_e32 v14, 8, v14
	v_cndmask_b32_e64 v14, v14, v233, s[28:29]
	v_lshl_add_u32 v14, v14, 2, v222
	ds_add_u32 v14, v224 offset:36864
	v_bitop3_b32 v14, v15, s7, v15 bitop3:0xc
	v_or_b32_e32 v24, 0x8000, v15
	v_cmp_gt_i16_e32 vcc, 0, v15
	v_or_b32_e32 v15, 0x8000, v12
	v_cvt_f16_f32_e32 v13, v13
	v_cndmask_b32_e32 v14, v24, v14, vcc
	v_cndmask_b32_e64 v24, v14, 0, s[30:31]
	v_lshrrev_b32_e32 v14, 8, v14
	v_cndmask_b32_e64 v14, v14, v233, s[30:31]
	v_lshl_add_u32 v14, v14, 2, v222
	ds_add_u32 v14, v224 offset:36864
	v_bitop3_b32 v14, v12, s7, v12 bitop3:0xc
	v_cmp_gt_i16_e32 vcc, 0, v12
	v_cvt_f16_f32_e32 v10, v10
	v_cvt_f16_f32_e32 v11, v11
	v_cndmask_b32_e32 v12, v15, v14, vcc
	v_cndmask_b32_e64 v25, v12, 0, s[34:35]
	v_lshrrev_b32_e32 v12, 8, v12
	v_cndmask_b32_e64 v12, v12, v233, s[34:35]
	v_lshl_add_u32 v12, v12, 2, v222
	ds_add_u32 v12, v224 offset:36864
	v_bitop3_b32 v12, v13, s7, v13 bitop3:0xc
	v_or_b32_e32 v14, 0x8000, v13
	v_cmp_gt_i16_e32 vcc, 0, v13
	v_or_b32_e32 v13, 0x8000, v10
	v_cvt_f16_f32_e32 v8, v8
	v_cndmask_b32_e32 v12, v14, v12, vcc
	v_cndmask_b32_e64 v27, v12, 0, s[36:37]
	v_lshrrev_b32_e32 v12, 8, v12
	v_cndmask_b32_e64 v12, v12, v233, s[36:37]
	v_lshl_add_u32 v12, v12, 2, v222
	ds_add_u32 v12, v224 offset:36864
	v_bitop3_b32 v12, v10, s7, v10 bitop3:0xc
	v_cmp_gt_i16_e32 vcc, 0, v10
	v_cvt_f16_f32_e32 v9, v9
	v_cvt_f16_f32_e32 v6, v6
	v_cndmask_b32_e32 v10, v13, v12, vcc
	v_cndmask_b32_e64 v28, v10, 0, s[38:39]
	v_lshrrev_b32_e32 v10, 8, v10
	v_cndmask_b32_e64 v10, v10, v233, s[38:39]
	v_lshl_add_u32 v10, v10, 2, v222
	ds_add_u32 v10, v224 offset:36864
	v_bitop3_b32 v10, v11, s7, v11 bitop3:0xc
	v_or_b32_e32 v12, 0x8000, v11
	v_cmp_gt_i16_e32 vcc, 0, v11
	v_or_b32_e32 v11, 0x8000, v8
	v_cvt_f16_f32_e32 v7, v7
	v_cndmask_b32_e32 v10, v12, v10, vcc
	v_cndmask_b32_e64 v32, v10, 0, s[40:41]
	v_lshrrev_b32_e32 v10, 8, v10
	v_cndmask_b32_e64 v10, v10, v233, s[40:41]
	v_lshl_add_u32 v10, v10, 2, v222
	ds_add_u32 v10, v224 offset:36864
	v_bitop3_b32 v10, v8, s7, v8 bitop3:0xc
	v_cmp_gt_i16_e32 vcc, 0, v8
	v_cvt_f16_f32_e32 v4, v4
	v_cvt_f16_f32_e32 v5, v5
	v_cndmask_b32_e32 v8, v11, v10, vcc
	v_cndmask_b32_e64 v33, v8, 0, s[42:43]
	v_lshrrev_b32_e32 v8, 8, v8
	v_cndmask_b32_e64 v8, v8, v233, s[42:43]
	v_lshl_add_u32 v8, v8, 2, v222
	ds_add_u32 v8, v224 offset:36864
	v_bitop3_b32 v8, v9, s7, v9 bitop3:0xc
	v_or_b32_e32 v10, 0x8000, v9
	v_cmp_gt_i16_e32 vcc, 0, v9
	v_or_b32_e32 v9, 0x8000, v6
	v_cndmask_b32_e64 v42, v26, 0, s[24:25]
	v_cndmask_b32_e32 v8, v10, v8, vcc
	v_cndmask_b32_e64 v34, v8, 0, s[44:45]
	v_lshrrev_b32_e32 v8, 8, v8
	v_cndmask_b32_e64 v8, v8, v233, s[44:45]
	v_lshl_add_u32 v8, v8, 2, v222
	ds_add_u32 v8, v224 offset:36864
	v_bitop3_b32 v8, v6, s7, v6 bitop3:0xc
	v_cmp_gt_i16_e32 vcc, 0, v6
	v_mov_b32_e32 v26, v42
	s_nop 0
	v_cndmask_b32_e32 v6, v9, v8, vcc
	v_cndmask_b32_e64 v35, v6, 0, s[46:47]
	v_lshrrev_b32_e32 v6, 8, v6
	v_cndmask_b32_e64 v6, v6, v233, s[46:47]
	v_lshl_add_u32 v6, v6, 2, v222
	ds_add_u32 v6, v224 offset:36864
	v_bitop3_b32 v6, v7, s7, v7 bitop3:0xc
	v_or_b32_e32 v8, 0x8000, v7
	v_cmp_gt_i16_e32 vcc, 0, v7
	v_or_b32_e32 v7, 0x8000, v4
	s_nop 0
	v_cndmask_b32_e32 v6, v8, v6, vcc
	v_cndmask_b32_e64 v36, v6, 0, s[48:49]
	v_lshrrev_b32_e32 v6, 8, v6
	v_cndmask_b32_e64 v6, v6, v233, s[48:49]
	v_lshl_add_u32 v6, v6, 2, v222
	ds_add_u32 v6, v224 offset:36864
	v_bitop3_b32 v6, v4, s7, v4 bitop3:0xc
	v_cmp_gt_i16_e32 vcc, 0, v4
	s_nop 1
	v_cndmask_b32_e32 v4, v7, v6, vcc
	v_cndmask_b32_e64 v37, v4, 0, s[50:51]
	v_lshrrev_b32_e32 v4, 8, v4
	v_cndmask_b32_e64 v4, v4, v233, s[50:51]
	v_lshl_add_u32 v4, v4, 2, v222
	ds_add_u32 v4, v224 offset:36864
	v_bitop3_b32 v4, v5, s7, v5 bitop3:0xc
	v_or_b32_e32 v6, 0x8000, v5
	v_cmp_gt_i16_e32 vcc, 0, v5
	s_nop 1
	v_cndmask_b32_e32 v4, v6, v4, vcc
	v_cndmask_b32_e64 v39, v4, 0, s[52:53]
	v_lshrrev_b32_e32 v4, 8, v4
	v_cndmask_b32_e64 v4, v4, v233, s[52:53]
	v_lshl_add_u32 v4, v4, 2, v222
	v_cmp_gt_i16_e32 vcc, 0, v18
	ds_add_u32 v4, v224 offset:36864
	s_nop 0
	v_cndmask_b32_e32 v4, v22, v21, vcc
	v_cndmask_b32_e64 v38, v4, 0, s[54:55]
	v_lshrrev_b32_e32 v4, 8, v4
	v_cndmask_b32_e64 v4, v4, v233, s[54:55]
	v_lshl_add_u32 v4, v4, 2, v222
	ds_add_u32 v4, v224 offset:36864
	v_cmp_gt_i16_e32 vcc, 0, v17
	s_nop 1
	v_cndmask_b32_e32 v4, v20, v19, vcc
	v_cndmask_b32_e64 v40, v4, 0, s[56:57]
	v_lshrrev_b32_e32 v4, 8, v4
	v_cndmask_b32_e64 v41, v4, v233, s[56:57]

.Lst_382:
	s_cmp_eq_u32 s81, s0
	s_mov_b64 s[0:1], -1
	v_mfma_f32_32x32x16_bf16 v[10:25], v[68:71], v[84:87], 0
	v_mfma_f32_32x32x16_bf16 v[10:25], v[64:67], v[88:91], v[10:25]
	v_mfma_f32_32x32x16_bf16 v[10:25], v[60:63], v[92:95], v[10:25]
	v_mfma_f32_32x32x16_bf16 v[10:25], v[56:59], v[96:99], v[10:25]
	s_nop 11
	v_fma_f32 v48, |v10|, v2, 0
	v_fma_f32 v49, |v11|, v2, 0
	v_fma_f32 v50, |v12|, v2, 0
	v_fma_f32 v51, |v13|, v2, 0
	v_fma_f32 v212, |v14|, v2, 0
	v_fma_f32 v213, |v15|, v2, 0
	v_fma_f32 v215, |v16|, v2, 0
	v_fma_f32 v216, |v17|, v2, 0
	v_fma_f32 v217, |v18|, v2, 0
	v_fma_f32 v228, |v19|, v2, 0
	v_mfma_f32_32x32x16_bf16 v[4:19], v[68:71], v[100:103], 0
	v_fma_f32 v229, |v20|, v2, 0
	v_fma_f32 v230, |v21|, v2, 0
	v_mfma_f32_32x32x16_bf16 v[4:19], v[64:67], v[104:107], v[4:19]
	v_fma_f32 v234, |v22|, v2, 0
	v_fma_f32 v235, |v23|, v2, 0
	v_mfma_f32_32x32x16_bf16 v[4:19], v[60:63], v[108:111], v[4:19]
	v_fma_f32 v236, |v24|, v2, 0
	v_fma_f32 v237, |v25|, v2, 0
	v_mfma_f32_32x32x16_bf16 v[4:19], v[56:59], v[112:115], v[4:19]
	s_nop 11
	v_fma_f32 v48, |v4|, v249, v48
	v_mfma_f32_32x32x16_bf16 v[20:35], v[68:71], v[116:119], 0
	v_fma_f32 v49, |v5|, v249, v49
	v_fma_f32 v50, |v6|, v249, v50
	v_fma_f32 v51, |v7|, v249, v51
	v_mfma_f32_32x32x16_bf16 v[20:35], v[64:67], v[120:123], v[20:35]
	v_fma_f32 v8, |v8|, v249, v212
	v_fma_f32 v9, |v9|, v249, v213
	v_fma_f32 v10, |v10|, v249, v215
	v_fma_f32 v11, |v11|, v249, v216
	v_mfma_f32_32x32x16_bf16 v[20:35], v[60:63], v[124:127], v[20:35]
	v_fma_f32 v12, |v12|, v249, v217
	v_fma_f32 v13, |v13|, v249, v228
	v_fma_f32 v212, |v14|, v249, v229
	v_fma_f32 v213, |v15|, v249, v230
	v_fma_f32 v215, |v16|, v249, v234
	v_fma_f32 v216, |v17|, v249, v235
	v_fma_f32 v217, |v18|, v249, v236
	v_fma_f32 v228, |v19|, v249, v237
	v_mfma_f32_32x32x16_bf16 v[20:35], v[56:59], v[128:131], v[20:35]
	s_nop 11
	v_fma_f32 v24, |v24|, v250, v8
	v_fma_f32 v25, |v25|, v250, v9
	v_fma_f32 v26, |v26|, v250, v10
	v_fma_f32 v27, |v27|, v250, v11
	v_fma_f32 v28, |v28|, v250, v12
	v_fma_f32 v29, |v29|, v250, v13
	v_mfma_f32_32x32x16_bf16 v[4:19], v[68:71], v[132:135], 0
	v_fma_f32 v48, |v20|, v250, v48
	v_fma_f32 v49, |v21|, v250, v49
	v_fma_f32 v50, |v22|, v250, v50
	v_fma_f32 v51, |v23|, v250, v51
	v_mfma_f32_32x32x16_bf16 v[4:19], v[64:67], v[136:139], v[4:19]
	v_fma_f32 v212, |v30|, v250, v212
	v_mfma_f32_32x32x16_bf16 v[4:19], v[60:63], v[140:143], v[4:19]
	v_fma_f32 v213, |v31|, v250, v213
	v_fma_f32 v215, |v32|, v250, v215
	v_fma_f32 v216, |v33|, v250, v216
	v_fma_f32 v217, |v34|, v250, v217
	v_fma_f32 v228, |v35|, v250, v228
	v_mfma_f32_32x32x16_bf16 v[4:19], v[56:59], v[144:147], v[4:19]
	s_nop 11
	v_fma_f32 v229, |v8|, v251, v24
	v_fma_f32 v230, |v9|, v251, v25
	v_fma_f32 v234, |v10|, v251, v26
	v_fma_f32 v235, |v11|, v251, v27
	v_fma_f32 v236, |v12|, v251, v28
	v_fma_f32 v237, |v13|, v251, v29
	v_mfma_f32_32x32x16_bf16 v[20:35], v[68:71], v[148:151], 0
	v_fma_f32 v48, |v4|, v251, v48
	v_fma_f32 v49, |v5|, v251, v49
	v_fma_f32 v50, |v6|, v251, v50
	v_fma_f32 v51, |v7|, v251, v51
	v_mfma_f32_32x32x16_bf16 v[20:35], v[64:67], v[152:155], v[20:35]
	v_fma_f32 v212, |v14|, v251, v212
	v_mfma_f32_32x32x16_bf16 v[20:35], v[60:63], v[156:159], v[20:35]
	v_fma_f32 v213, |v15|, v251, v213
	v_fma_f32 v215, |v16|, v251, v215
	v_fma_f32 v216, |v17|, v251, v216
	v_fma_f32 v217, |v18|, v251, v217
	v_fma_f32 v228, |v19|, v251, v228
	v_mfma_f32_32x32x16_bf16 v[20:35], v[56:59], v[160:163], v[20:35]
	s_nop 11
	v_fma_f32 v20, |v20|, v252, v48
	v_fma_f32 v21, |v21|, v252, v49
	v_fma_f32 v22, |v22|, v252, v50
	v_fma_f32 v23, |v23|, v252, v51
	v_mfma_f32_32x32x16_bf16 v[36:51], v[68:71], v[164:167], 0
	v_fma_f32 v24, |v24|, v252, v229
	v_fma_f32 v25, |v25|, v252, v230
	v_mfma_f32_32x32x16_bf16 v[36:51], v[64:67], v[168:171], v[36:51]
	v_fma_f32 v26, |v26|, v252, v234
	v_fma_f32 v27, |v27|, v252, v235
	v_mfma_f32_32x32x16_bf16 v[36:51], v[60:63], v[172:175], v[36:51]
	v_fma_f32 v229, |v28|, v252, v236
	v_fma_f32 v230, |v29|, v252, v237
	v_fma_f32 v212, |v30|, v252, v212
	v_fma_f32 v213, |v31|, v252, v213
	v_fma_f32 v215, |v32|, v252, v215
	v_fma_f32 v216, |v33|, v252, v216
	v_fma_f32 v217, |v34|, v252, v217
	v_fma_f32 v228, |v35|, v252, v228
	v_mfma_f32_32x32x16_bf16 v[36:51], v[56:59], v[176:179], v[36:51]
	s_nop 11
	v_fma_f32 v234, |v36|, v253, v20
	v_fma_f32 v235, |v37|, v253, v21
	v_fma_f32 v236, |v38|, v253, v22
	v_fma_f32 v237, |v39|, v253, v23
	v_fma_f32 v40, |v40|, v253, v24
	v_fma_f32 v41, |v41|, v253, v25
	v_fma_f32 v42, |v42|, v253, v26
	v_fma_f32 v43, |v43|, v253, v27
	v_mfma_f32_32x32x16_bf16 v[12:27], v[68:71], v[180:183], 0
	v_fma_f32 v44, |v44|, v253, v229
	v_fma_f32 v45, |v45|, v253, v230
	v_mfma_f32_32x32x16_bf16 v[12:27], v[64:67], v[184:187], v[12:27]
	v_fma_f32 v46, |v46|, v253, v212
	v_fma_f32 v47, |v47|, v253, v213
	v_mfma_f32_32x32x16_bf16 v[12:27], v[60:63], v[188:191], v[12:27]
	v_fma_f32 v48, |v48|, v253, v215
	v_fma_f32 v49, |v49|, v253, v216
	v_fma_f32 v50, |v50|, v253, v217
	v_fma_f32 v51, |v51|, v253, v228
	v_mfma_f32_32x32x16_bf16 v[12:27], v[56:59], v[192:195], v[12:27]
	s_nop 11
	v_fma_f32 v212, |v12|, v223, v234
	v_fma_f32 v213, |v13|, v223, v235
	v_fma_f32 v215, |v14|, v223, v236
	v_fma_f32 v216, |v15|, v223, v237
	v_fma_f32 v217, |v16|, v223, v40
	v_fma_f32 v228, |v17|, v223, v41
	v_fma_f32 v229, |v18|, v223, v42
	v_fma_f32 v230, |v19|, v223, v43
	v_mfma_f32_32x32x16_bf16 v[4:19], v[68:71], v[196:199], 0
	v_fma_f32 v234, |v20|, v223, v44
	v_fma_f32 v235, |v21|, v223, v45
	v_mfma_f32_32x32x16_bf16 v[4:19], v[64:67], v[200:203], v[4:19]
	v_fma_f32 v236, |v22|, v223, v46
	v_fma_f32 v237, |v23|, v223, v47
	v_mfma_f32_32x32x16_bf16 v[4:19], v[60:63], v[204:207], v[4:19]
	v_fma_f32 v48, |v24|, v223, v48
	v_fma_f32 v49, |v25|, v223, v49
	v_fma_f32 v50, |v26|, v223, v50
	v_fma_f32 v51, |v27|, v223, v51
	v_mfma_f32_32x32x16_bf16 v[4:19], v[56:59], v[208:211], v[4:19]
	ds_read_b128 v[20:23], v214 offset:32768
	ds_read_b128 v[36:39], v214 offset:33792
	ds_read_b128 v[40:43], v214 offset:34816
	ds_read_b128 v[44:47], v214 offset:35840
	s_waitcnt lgkmcnt(3)
	v_mfma_f32_32x32x16_bf16 v[20:35], v[68:71], v[20:23], 0
	s_nop 5
	v_fma_f32 v212, |v4|, v219, v212
	v_fma_f32 v213, |v5|, v219, v213
	v_fma_f32 v4, |v6|, v219, v215
	v_fma_f32 v5, |v7|, v219, v216
	s_waitcnt lgkmcnt(2)
	v_mfma_f32_32x32x16_bf16 v[20:35], v[64:67], v[36:39], v[20:35]
	v_fma_f32 v6, |v8|, v219, v217
	v_fma_f32 v7, |v9|, v219, v228
	v_fma_f32 v8, |v10|, v219, v229
	v_fma_f32 v9, |v11|, v219, v230
	s_waitcnt lgkmcnt(1)
	v_mfma_f32_32x32x16_bf16 v[20:35], v[60:63], v[40:43], v[20:35]
	v_fma_f32 v36, |v12|, v219, v234
	v_fma_f32 v37, |v13|, v219, v235
	v_fma_f32 v38, |v14|, v219, v236
	v_fma_f32 v39, |v15|, v219, v237
	s_waitcnt lgkmcnt(0)
	v_mfma_f32_32x32x16_bf16 v[20:35], v[56:59], v[44:47], v[20:35]
	v_fma_f32 v16, |v16|, v219, v48
	v_fma_f32 v17, |v17|, v219, v49
	s_nop 9
	v_add_f32_e32 v20, v212, v20
	v_pk_add_f32 v[14:15], v[4:5], v[22:23]
	v_pk_add_f32 v[4:5], v[32:33], v[16:17]
	v_cvt_f16_f32_e32 v16, v20
	v_fma_f32 v18, |v18|, v219, v50
	v_fma_f32 v19, |v19|, v219, v51
	v_add_f32_e32 v21, v213, v21
	v_add_f32_e32 v17, v34, v18
	v_add_f32_e32 v19, v35, v19
	v_pk_add_f32 v[10:11], v[8:9], v[26:27]
	v_pk_add_f32 v[8:9], v[36:37], v[28:29]
	v_cvt_f16_f32_e32 v29, v21
	v_cvt_f16_f32_e32 v18, v17
	v_cvt_f16_f32_e32 v17, v19
	v_pk_add_f32 v[12:13], v[6:7], v[24:25]
	v_pk_add_f32 v[6:7], v[38:39], v[30:31]
	s_cbranch_scc1 .Lst_384
	s_mov_b64 s[0:1], 0
	v_cvt_pk_f16_f32 v23, v6, v7
	v_pk_ashrrev_i16 v24, 15, v23 op_sel_hi:[0,1]
	v_bitop3_b32 v7, v23, v24, s32 bitop3:0x1e
	v_bfe_u32 v24, v7, 8, 8
	v_lshrrev_b32_e32 v23, 24, v7
	v_lshl_add_u32 v24, v24, 2, v222
	v_lshl_add_u32 v23, v23, 2, v222
	ds_add_u32 v24, v224 offset:36864
	ds_add_u32 v23, v224 offset:36864
	v_cvt_pk_f16_f32 v25, v8, v9
	v_pk_ashrrev_i16 v27, 15, v25 op_sel_hi:[0,1]
	v_bitop3_b32 v6, v25, v27, s32 bitop3:0x1e
	v_bfe_u32 v27, v6, 8, 8
	v_lshrrev_b32_e32 v25, 24, v6
	v_lshl_add_u32 v27, v27, 2, v222
	v_lshl_add_u32 v25, v25, 2, v222
	ds_add_u32 v27, v224 offset:36864
	ds_add_u32 v25, v224 offset:36864
	v_cvt_pk_f16_f32 v28, v10, v11
	v_pk_ashrrev_i16 v32, 15, v28 op_sel_hi:[0,1]
	v_bitop3_b32 v9, v28, v32, s32 bitop3:0x1e
	v_bfe_u32 v32, v9, 8, 8
	v_lshrrev_b32_e32 v28, 24, v9
	v_lshl_add_u32 v32, v32, 2, v222
	v_lshl_add_u32 v28, v28, 2, v222
	ds_add_u32 v32, v224 offset:36864
	ds_add_u32 v28, v224 offset:36864
	v_cvt_pk_f16_f32 v33, v12, v13
	v_pk_ashrrev_i16 v34, 15, v33 op_sel_hi:[0,1]
	v_bitop3_b32 v8, v33, v34, s32 bitop3:0x1e
	v_bfe_u32 v34, v8, 8, 8
	v_lshrrev_b32_e32 v33, 24, v8
	v_lshl_add_u32 v34, v34, 2, v222
	v_lshl_add_u32 v33, v33, 2, v222
	ds_add_u32 v34, v224 offset:36864
	ds_add_u32 v33, v224 offset:36864
	v_cvt_pk_f16_f32 v35, v4, v5
	v_pk_ashrrev_i16 v36, 15, v35 op_sel_hi:[0,1]
	v_bitop3_b32 v10, v35, v36, s32 bitop3:0x1e
	v_bfe_u32 v36, v10, 8, 8
	v_lshrrev_b32_e32 v35, 24, v10
	v_lshl_add_u32 v36, v36, 2, v222
	v_lshl_add_u32 v35, v35, 2, v222
	ds_add_u32 v36, v224 offset:36864
	ds_add_u32 v35, v224 offset:36864
	v_cvt_pk_f16_f32 v37, v14, v15
	v_pk_ashrrev_i16 v39, 15, v37 op_sel_hi:[0,1]
	v_bitop3_b32 v5, v37, v39, s32 bitop3:0x1e
	v_bfe_u32 v39, v5, 8, 8
	v_lshrrev_b32_e32 v37, 24, v5
	v_lshl_add_u32 v39, v39, 2, v222
	v_lshl_add_u32 v37, v37, 2, v222
	ds_add_u32 v39, v224 offset:36864
	ds_add_u32 v37, v224 offset:36864
	v_lshl_or_b32 v23, v29, 16, v16
	v_lshl_or_b32 v25, v17, 16, v18
	v_pk_ashrrev_i16 v24, 15, v23 op_sel_hi:[0,1]
	v_pk_ashrrev_i16 v27, 15, v25 op_sel_hi:[0,1]
	v_bitop3_b32 v4, v23, v24, s32 bitop3:0x1e
	v_bitop3_b32 v11, v25, v27, s32 bitop3:0x1e
	v_bfe_u32 v23, v4, 8, 8
	v_lshrrev_b32_e32 v24, 24, v4
	v_bfe_u32 v25, v11, 8, 8
	v_lshrrev_b32_e32 v27, 24, v11
	v_lshl_add_u32 v23, v23, 2, v222
	v_lshl_add_u32 v24, v24, 2, v222
	v_lshl_add_u32 v25, v25, 2, v222
	v_lshl_add_u32 v27, v27, 2, v222
	ds_add_u32 v23, v224 offset:36864
	ds_add_u32 v24, v224 offset:36864
	ds_add_u32 v25, v224 offset:36864
	ds_add_u32 v27, v224 offset:36864
	s_branch .Lidx_join_b
